# E19: E15 + wave-group-0 K-loop exit barrier deferred to just before the epilogue parameter wait in G1/G2/w_out GEMM (group 0 issues its epilogue loads during group 1's last MFMA phase)
# speedup vs baseline: 1.0083x; 1.0072x over previous
.Lkexit_982:
.LBB0_985:
	v_lshl_add_u32 v150, s16, 8, v1
	v_lshl_or_b32 v146, s40, 8, v153
	v_or_b32_e32 v222, 16, v150
	v_ashrrev_i32_e32 v147, 31, v146
	v_ashrrev_i32_e32 v151, 31, v150
	v_ashrrev_i32_e32 v223, 31, v222
	v_lshl_add_u64 v[148:149], v[146:147], 2, s[68:69]
	v_lshlrev_b64 v[158:159], 13, v[150:151]
	v_lshlrev_b64 v[174:175], 13, v[222:223]
	v_or_b32_e32 v224, 32, v150
	v_lshl_add_u64 v[170:171], v[148:149], 0, v[158:159]
	v_lshl_add_u64 v[186:187], v[148:149], 0, v[174:175]
	v_ashrrev_i32_e32 v225, 31, v224
	global_load_dwordx4 v[158:161], v[170:171], off
	global_load_dwordx4 v[162:165], v[170:171], off offset:16
	global_load_dwordx4 v[166:169], v[170:171], off offset:512
	s_nop 0
	global_load_dwordx4 v[170:173], v[170:171], off offset:528
	s_nop 0
	global_load_dwordx4 v[174:177], v[186:187], off
	global_load_dwordx4 v[178:181], v[186:187], off offset:16
	v_lshlrev_b64 v[190:191], 13, v[224:225]
	global_load_dwordx4 v[182:185], v[186:187], off offset:528
	s_nop 0
	global_load_dwordx4 v[186:189], v[186:187], off offset:512
	v_lshl_add_u64 v[202:203], v[148:149], 0, v[190:191]
	global_load_dwordx4 v[190:193], v[202:203], off
	global_load_dwordx4 v[194:197], v[202:203], off offset:16
	global_load_dwordx4 v[198:201], v[202:203], off offset:512
	s_nop 0
	global_load_dwordx4 v[202:205], v[202:203], off offset:528
	v_or_b32_e32 v228, 48, v150
	v_ashrrev_i32_e32 v229, 31, v228
	v_lshlrev_b64 v[206:207], 13, v[228:229]
	v_lshl_add_u64 v[218:219], v[148:149], 0, v[206:207]
	global_load_dwordx4 v[206:209], v[218:219], off
	global_load_dwordx4 v[210:213], v[218:219], off offset:16
	global_load_dwordx4 v[214:217], v[218:219], off offset:512
	s_nop 0
	global_load_dwordx4 v[218:221], v[218:219], off offset:528
	v_readlane_b32 s18, v253, 40
	v_lshlrev_b64 v[230:231], 12, v[150:151]
	v_readlane_b32 s19, v253, 41
	v_lshlrev_b64 v[222:223], 12, v[222:223]
	v_lshlrev_b64 v[146:147], 1, v[146:147]
	v_lshl_add_u64 v[230:231], s[18:19], 0, v[230:231]
	v_lshl_add_u64 v[222:223], s[18:19], 0, v[222:223]
	v_lshlrev_b64 v[224:225], 12, v[224:225]
	v_lshl_add_u64 v[230:231], v[230:231], 0, v[146:147]
	v_lshl_add_u64 v[222:223], v[222:223], 0, v[146:147]
	v_lshl_add_u64 v[224:225], s[18:19], 0, v[224:225]
	s_andn2_b64 vcc, exec, s[4:5]
	s_mov_b64 s[4:5], -1
	s_and_b64 s[98:99], exec, s[6:7]
	s_cbranch_scc0 .Lepi_nb_982
	s_barrier
.Lepi_nb_982:
	s_waitcnt vmcnt(0)
	v_pk_add_f32 v[128:129], v[128:129], v[160:161]
	v_pk_add_f32 v[126:127], v[126:127], v[158:159]
	v_pk_add_f32 v[124:125], v[124:125], v[164:165]
	v_pk_add_f32 v[122:123], v[122:123], v[162:163]
	v_pk_add_f32 v[120:121], v[120:121], v[176:177]
	v_pk_add_f32 v[118:119], v[118:119], v[174:175]
	v_pk_add_f32 v[116:117], v[116:117], v[180:181]
	v_pk_add_f32 v[114:115], v[114:115], v[178:179]
	v_pk_add_f32 v[112:113], v[112:113], v[168:169]
	v_pk_add_f32 v[110:111], v[110:111], v[166:167]
	v_pk_add_f32 v[158:159], v[104:105], v[172:173]
	v_pk_add_f32 v[160:161], v[102:103], v[170:171]
	v_cvt_pk_bf16_f32 v102, v126, v127
	v_cvt_pk_bf16_f32 v103, v128, v129
	v_cvt_pk_bf16_f32 v104, v122, v123
	v_cvt_pk_bf16_f32 v105, v124, v125
	v_pk_add_f32 v[96:97], v[96:97], v[188:189]
	v_pk_add_f32 v[94:95], v[94:95], v[186:187]
	v_pk_add_f32 v[122:123], v[92:93], v[184:185]
	v_pk_add_f32 v[124:125], v[90:91], v[182:183]
	v_cvt_pk_bf16_f32 v90, v118, v119
	v_cvt_pk_bf16_f32 v91, v120, v121
	v_cvt_pk_bf16_f32 v92, v114, v115
	v_cvt_pk_bf16_f32 v93, v116, v117
	v_cvt_pk_bf16_f32 v110, v110, v111
	v_cvt_pk_bf16_f32 v111, v112, v113
	v_cvt_pk_bf16_f32 v112, v160, v161
	v_cvt_pk_bf16_f32 v113, v158, v159
	global_store_dwordx4 v[230:231], v[102:105], off
	global_store_dwordx4 v[230:231], v[110:113], off offset:256
	v_cvt_pk_bf16_f32 v94, v94, v95
	v_cvt_pk_bf16_f32 v95, v96, v97
	v_cvt_pk_bf16_f32 v96, v124, v125
	v_cvt_pk_bf16_f32 v97, v122, v123
	global_store_dwordx4 v[222:223], v[90:93], off
	global_store_dwordx4 v[222:223], v[94:97], off offset:256
	v_pk_add_f32 v[84:85], v[84:85], v[200:201]
	v_pk_add_f32 v[82:83], v[82:83], v[198:199]
	v_pk_add_f32 v[92:93], v[76:77], v[204:205]
	v_pk_add_f32 v[76:77], v[74:75], v[202:203]
	v_lshl_add_u64 v[90:91], v[224:225], 0, v[146:147]
	v_cvt_pk_bf16_f32 v74, v82, v83
	v_cvt_pk_bf16_f32 v75, v84, v85
	v_cvt_pk_bf16_f32 v76, v76, v77
	v_cvt_pk_bf16_f32 v77, v92, v93
	global_store_dwordx4 v[90:91], v[74:77], off offset:256
	v_lshlrev_b64 v[82:83], 12, v[228:229]
	v_pk_add_f32 v[78:79], v[78:79], v[210:211]
	v_pk_add_f32 v[76:77], v[88:89], v[208:209]
	v_pk_add_f32 v[74:75], v[86:87], v[206:207]
	v_pk_add_f32 v[80:81], v[80:81], v[212:213]
	v_cvt_pk_bf16_f32 v74, v74, v75
	v_cvt_pk_bf16_f32 v75, v76, v77
	v_cvt_pk_bf16_f32 v76, v78, v79
	v_lshl_add_u64 v[78:79], s[18:19], 0, v[82:83]
	v_cvt_pk_bf16_f32 v77, v80, v81
	v_lshl_add_u64 v[78:79], v[78:79], 0, v[146:147]
	global_store_dwordx4 v[78:79], v[74:77], off
	v_pk_add_f32 v[72:73], v[72:73], v[216:217]
	v_pk_add_f32 v[70:71], v[70:71], v[214:215]
	v_pk_add_f32 v[74:75], v[68:69], v[220:221]
	v_pk_add_f32 v[68:69], v[66:67], v[218:219]
	v_add_u32_e32 v158, 0x80, v150
	v_pk_add_f32 v[108:109], v[108:109], v[192:193]
	v_pk_add_f32 v[106:107], v[106:107], v[190:191]
	v_pk_add_f32 v[126:127], v[100:101], v[196:197]
	v_pk_add_f32 v[100:101], v[98:99], v[194:195]
	v_cvt_pk_bf16_f32 v66, v70, v71
	v_cvt_pk_bf16_f32 v67, v72, v73
	v_cvt_pk_bf16_f32 v68, v68, v69
	v_cvt_pk_bf16_f32 v69, v74, v75
	v_ashrrev_i32_e32 v159, 31, v158
	v_cvt_pk_bf16_f32 v98, v106, v107
	v_cvt_pk_bf16_f32 v99, v108, v109
	v_cvt_pk_bf16_f32 v100, v100, v101
	v_cvt_pk_bf16_f32 v101, v126, v127
	global_store_dwordx4 v[78:79], v[66:69], off offset:256
	global_store_dwordx4 v[90:91], v[98:101], off
	v_add_u32_e32 v160, 0x90, v150
	v_lshlrev_b64 v[66:67], 13, v[158:159]
	v_lshl_add_u64 v[78:79], v[148:149], 0, v[66:67]
	global_load_dwordx4 v[66:69], v[78:79], off
	global_load_dwordx4 v[70:73], v[78:79], off offset:16
	global_load_dwordx4 v[74:77], v[78:79], off offset:512
	s_nop 0
	global_load_dwordx4 v[78:81], v[78:79], off offset:528
	v_ashrrev_i32_e32 v161, 31, v160
	v_lshlrev_b64 v[82:83], 13, v[160:161]
	v_lshl_add_u64 v[94:95], v[148:149], 0, v[82:83]
	global_load_dwordx4 v[82:85], v[94:95], off
	global_load_dwordx4 v[86:89], v[94:95], off offset:16
	global_load_dwordx4 v[90:93], v[94:95], off offset:512
	s_nop 0
	global_load_dwordx4 v[94:97], v[94:95], off offset:528
	v_add_u32_e32 v162, 0xa0, v150
	v_ashrrev_i32_e32 v163, 31, v162
	v_lshlrev_b64 v[98:99], 13, v[162:163]
	v_lshl_add_u64 v[110:111], v[148:149], 0, v[98:99]
	global_load_dwordx4 v[98:101], v[110:111], off
	global_load_dwordx4 v[102:105], v[110:111], off offset:16
	global_load_dwordx4 v[106:109], v[110:111], off offset:512
	s_nop 0
	global_load_dwordx4 v[110:113], v[110:111], off offset:528
	v_add_u32_e32 v150, 0xb0, v150
	v_ashrrev_i32_e32 v151, 31, v150
	v_lshlrev_b64 v[114:115], 13, v[150:151]
	v_lshl_add_u64 v[126:127], v[148:149], 0, v[114:115]
	global_load_dwordx4 v[114:117], v[126:127], off
	global_load_dwordx4 v[118:121], v[126:127], off offset:16
	global_load_dwordx4 v[122:125], v[126:127], off offset:512
	s_nop 0
	global_load_dwordx4 v[126:129], v[126:127], off offset:528
	v_lshlrev_b64 v[148:149], 12, v[158:159]
	v_lshl_add_u64 v[148:149], s[18:19], 0, v[148:149]
	v_lshl_add_u64 v[148:149], v[148:149], 0, v[146:147]
	s_waitcnt vmcnt(15)
	v_pk_add_f32 v[64:65], v[64:65], v[68:69]
	v_pk_add_f32 v[62:63], v[62:63], v[66:67]
	s_waitcnt vmcnt(14)
	v_pk_add_f32 v[60:61], v[60:61], v[72:73]
	v_pk_add_f32 v[58:59], v[58:59], v[70:71]
	s_waitcnt vmcnt(12)
	v_pk_add_f32 v[66:67], v[48:49], v[80:81]
	v_pk_add_f32 v[68:69], v[46:47], v[78:79]
	v_cvt_pk_bf16_f32 v46, v62, v63
	v_cvt_pk_bf16_f32 v47, v64, v65
	v_cvt_pk_bf16_f32 v48, v58, v59
	v_cvt_pk_bf16_f32 v49, v60, v61
	global_store_dwordx4 v[148:149], v[46:49], off
	s_waitcnt vmcnt(12)
	v_pk_add_f32 v[50:51], v[50:51], v[82:83]
	s_waitcnt vmcnt(10)
	v_pk_add_f32 v[36:37], v[36:37], v[92:93]
	v_lshlrev_b64 v[46:47], 12, v[160:161]
	v_pk_add_f32 v[48:49], v[52:53], v[84:85]
	v_pk_add_f32 v[52:53], v[44:45], v[88:89]
	v_pk_add_f32 v[44:45], v[42:43], v[86:87]
	v_lshl_add_u64 v[46:47], s[18:19], 0, v[46:47]
	v_cvt_pk_bf16_f32 v42, v50, v51
	v_cvt_pk_bf16_f32 v43, v48, v49
	v_cvt_pk_bf16_f32 v44, v44, v45
	v_cvt_pk_bf16_f32 v45, v52, v53
	v_lshl_add_u64 v[46:47], v[46:47], 0, v[146:147]
	global_store_dwordx4 v[46:47], v[42:45], off
	v_pk_add_f32 v[34:35], v[34:35], v[90:91]
	s_waitcnt vmcnt(8)
	v_pk_add_f32 v[30:31], v[30:31], v[102:103]
	v_pk_add_f32 v[42:43], v[28:29], v[96:97]
	v_pk_add_f32 v[28:29], v[26:27], v[94:95]
	v_cvt_pk_bf16_f32 v26, v34, v35
	v_cvt_pk_bf16_f32 v27, v36, v37
	v_cvt_pk_bf16_f32 v28, v28, v29
	v_cvt_pk_bf16_f32 v29, v42, v43
	global_store_dwordx4 v[46:47], v[26:29], off offset:256
	v_lshlrev_b64 v[34:35], 12, v[162:163]
	v_pk_add_f32 v[32:33], v[32:33], v[104:105]
	v_pk_add_f32 v[28:29], v[40:41], v[100:101]
	v_pk_add_f32 v[26:27], v[38:39], v[98:99]
	s_waitcnt vmcnt(8)
	v_pk_add_f32 v[20:21], v[20:21], v[108:109]
	v_cvt_pk_bf16_f32 v26, v26, v27
	v_cvt_pk_bf16_f32 v27, v28, v29
	v_cvt_pk_bf16_f32 v28, v30, v31
	v_lshl_add_u64 v[30:31], s[18:19], 0, v[34:35]
	v_cvt_pk_bf16_f32 v29, v32, v33
	v_lshl_add_u64 v[30:31], v[30:31], 0, v[146:147]
	global_store_dwordx4 v[30:31], v[26:29], off
	v_pk_add_f32 v[18:19], v[18:19], v[106:107]
	s_waitcnt vmcnt(6)
	v_pk_add_f32 v[14:15], v[14:15], v[118:119]
	v_pk_add_f32 v[26:27], v[12:13], v[112:113]
	v_pk_add_f32 v[12:13], v[10:11], v[110:111]
	v_cvt_pk_bf16_f32 v10, v18, v19
	v_cvt_pk_bf16_f32 v11, v20, v21
	v_cvt_pk_bf16_f32 v12, v12, v13
	v_cvt_pk_bf16_f32 v13, v26, v27
	global_store_dwordx4 v[30:31], v[10:13], off offset:256
	v_lshlrev_b64 v[18:19], 12, v[150:151]
	v_pk_add_f32 v[16:17], v[16:17], v[120:121]
	v_pk_add_f32 v[12:13], v[24:25], v[116:117]
	v_pk_add_f32 v[10:11], v[22:23], v[114:115]
	v_pk_add_f32 v[56:57], v[56:57], v[76:77]
	v_cvt_pk_bf16_f32 v10, v10, v11
	v_cvt_pk_bf16_f32 v11, v12, v13
	v_cvt_pk_bf16_f32 v12, v14, v15
	v_lshl_add_u64 v[14:15], s[18:19], 0, v[18:19]
	v_cvt_pk_bf16_f32 v13, v16, v17
	v_lshl_add_u64 v[14:15], v[14:15], 0, v[146:147]
	v_pk_add_f32 v[54:55], v[54:55], v[74:75]
	global_store_dwordx4 v[14:15], v[10:13], off
	s_waitcnt vmcnt(7)
	v_pk_add_f32 v[8:9], v[8:9], v[124:125]
	v_pk_add_f32 v[6:7], v[6:7], v[122:123]
	s_waitcnt vmcnt(6)
	v_pk_add_f32 v[10:11], v[4:5], v[128:129]
	v_pk_add_f32 v[4:5], v[2:3], v[126:127]
	v_cvt_pk_bf16_f32 v54, v54, v55
	v_cvt_pk_bf16_f32 v55, v56, v57
	v_cvt_pk_bf16_f32 v56, v68, v69
	v_cvt_pk_bf16_f32 v57, v66, v67
	v_cvt_pk_bf16_f32 v2, v6, v7
	v_cvt_pk_bf16_f32 v3, v8, v9
	v_cvt_pk_bf16_f32 v4, v4, v5
	v_cvt_pk_bf16_f32 v5, v10, v11
	global_store_dwordx4 v[148:149], v[54:57], off offset:256
	global_store_dwordx4 v[14:15], v[2:5], off offset:256
	s_cbranch_vccnz .LBB0_974
	s_andn2_b64 vcc, exec, s[0:1]
	s_cbranch_vccnz .LBB0_973
	s_barrier
	s_branch .LBB0_973

.Lkexit_1214:
.LBB0_1217:
	s_add_i32 s35, s41, 2
	v_readlane_b32 s42, v252, 6
	s_mul_i32 s37, s35, s51
	v_readlane_b32 s43, v252, 7
	s_mul_hi_u32 s39, s35, s42
	s_add_i32 s39, s39, s37
	s_mul_i32 s35, s35, s42
	v_readlane_b32 s42, v252, 0
	v_readlane_b32 s43, v252, 1
	s_add_u32 s42, s35, s42
	s_addc_u32 s43, s39, s52
	v_cmp_ge_i64_e32 vcc, s[42:43], v[162:163]
	s_mov_b32 s44, s16
	s_cbranch_vccnz .LBB0_1219
	s_ashr_i32 s35, s42, 31
	s_lshr_b32 s35, s35, 29
	s_add_i32 s35, s42, s35
	s_ashr_i32 s37, s35, 3
	s_and_b32 s35, s35, -8
	s_sub_i32 s35, s42, s35
	s_cmp_lt_i32 s35, 0
	s_cselect_b32 s39, s66, s65
	s_mul_i32 s35, s35, s39
	s_add_i32 s35, s35, s37
	s_ashr_i32 s37, s35, 31
	s_lshr_b32 s37, s37, 25
	s_add_i32 s37, s35, s37
	s_ashr_i32 s39, s37, 7
	s_lshl_b32 s39, s39, 3
	s_sub_i32 s41, s31, s39
	s_min_i32 s41, s41, 8
	s_and_b32 s37, s37, 0xffffff80
	s_sub_i32 s35, s35, s37
	s_ashr_i32 s37, s35, 31
	s_abs_i32 s35, s35
	s_cmp_eq_u32 s41, 8
	s_cbranch_scc0 .Ldivslow_5
	s_and_b32 s35, s35, 7
	s_branch .Ldivjoin_5

.LBB0_1219:
	s_ashr_i32 s45, s44, 31
	s_lshl_b64 s[42:43], s[44:45], 9
	s_add_u32 s42, s55, s42
	v_mov_b32_e32 v0, v1
	s_addc_u32 s43, s56, s43
	global_load_dwordx2 v[172:173], v0, s[42:43]
	v_readlane_b32 s72, v252, 13
	s_ashr_i32 s41, s40, 31
	v_readlane_b32 s74, v252, 15
	v_readlane_b32 s75, v252, 16
	v_readlane_b32 s78, v252, 19
	v_readlane_b32 s79, v252, 20
	s_lshl_b64 s[40:41], s[40:41], 14
	s_mov_b64 s[74:75], s[78:79]
	v_lshl_or_b32 v176, s10, 7, v174
	s_add_u32 s42, s74, s40
	s_addc_u32 s43, s75, s41
	v_ashrrev_i32_e32 v177, 31, v176
	v_lshl_add_u64 v[78:79], v[176:177], 2, s[42:43]
	v_readlane_b32 s42, v252, 48
	v_readlane_b32 s43, v252, 49
	s_add_u32 s35, s42, s40
	s_addc_u32 s37, s43, s41
	s_lshl_b32 s40, s10, 8
	s_ashr_i32 s41, s40, 31
	s_lshl_b64 s[40:41], s[40:41], 2
	v_lshl_add_u32 v178, s16, 8, v188
	s_add_u32 s40, s35, s40
	v_ashrrev_i32_e32 v179, 31, v178
	s_addc_u32 s41, s37, s41
	v_lshlrev_b32_e32 v80, 2, v174
	v_lshl_add_u64 v[180:181], v[178:179], 2, s[20:21]
	global_load_dwordx4 v[70:73], v80, s[40:41] offset:16
	global_load_dwordx4 v[98:101], v80, s[40:41]
	global_load_dword v0, v[180:181], off
	global_load_dwordx4 v[74:77], v80, s[40:41] offset:528
	global_load_dwordx4 v[102:105], v80, s[40:41] offset:512
	global_load_dwordx4 v[106:109], v[78:79], off
	v_add_co_u32_e32 v80, vcc, s61, v78
	v_cvt_f32_i32_e32 v182, v158
	s_nop 0
	v_addc_co_u32_e32 v81, vcc, 0, v79, vcc
	global_load_dwordx4 v[94:97], v[80:81], off
	global_load_dwordx4 v[82:85], v[78:79], off offset:16
	v_lshl_add_u64 v[78:79], v[78:79], 0, s[28:29]
	global_load_dwordx4 v[78:81], v[78:79], off offset:16
	v_cvt_f32_i32_e32 v184, v154
	v_cvt_f32_i32_e32 v194, v160
	v_cvt_f32_i32_e32 v196, v156
	v_cvt_f32_i32_e32 v198, v150
	v_cvt_f32_i32_e32 v200, v146
	v_cvt_f32_i32_e32 v202, v152
	global_load_dword v160, v[180:181], off offset:64
	global_load_dword v158, v[180:181], off offset:128
	global_load_dword v156, v[180:181], off offset:192
	global_load_dword v154, v[180:181], off offset:512
	global_load_dword v152, v[180:181], off offset:576
	global_load_dword v150, v[180:181], off offset:640
	global_load_dword v146, v[180:181], off offset:704
	v_cvt_f32_i32_e32 v183, v159
	v_cvt_f32_i32_e32 v185, v155
	v_cvt_f32_i32_e32 v195, v161
	v_cvt_f32_i32_e32 v197, v157
	v_cvt_f32_i32_e32 v199, v151
	v_cvt_f32_i32_e32 v201, v147
	v_cvt_f32_i32_e32 v203, v153
	v_cvt_f32_i32_e32 v149, v149
	v_cvt_f32_i32_e32 v148, v148
	v_readlane_b32 s73, v252, 14
	v_readlane_b32 s76, v252, 17
	v_readlane_b32 s77, v252, 18
	v_readlane_b32 s80, v252, 21
	v_readlane_b32 s81, v252, 22
	v_readlane_b32 s82, v252, 23
	v_readlane_b32 s83, v252, 24
	v_readlane_b32 s84, v252, 25
	v_readlane_b32 s85, v252, 26
	v_readlane_b32 s86, v252, 27
	v_readlane_b32 s87, v252, 28
	s_and_b64 vcc, exec, s[26:27]
	s_cbranch_vccz .Lepi_nb_1214
	s_barrier
.Lepi_nb_1214:
	s_waitcnt vmcnt(0)
	v_pk_mul_f32 v[212:213], v[74:75], v[0:1] op_sel_hi:[1,0]
	v_pk_mul_f32 v[180:181], v[98:99], v[0:1] op_sel_hi:[1,0]
	v_pk_mul_f32 v[204:205], v[102:103], v[0:1] op_sel_hi:[1,0]
	v_pk_mul_f32 v[206:207], v[100:101], v[0:1] op_sel_hi:[1,0]
	v_pk_fma_f32 v[180:181], v[182:183], v[180:181], v[106:107]
	v_pk_mul_f32 v[208:209], v[104:105], v[0:1] op_sel_hi:[1,0]
	v_pk_mul_f32 v[210:211], v[70:71], v[0:1] op_sel_hi:[1,0]
	v_pk_fma_f32 v[182:183], v[184:185], v[204:205], v[94:95]
	v_pk_fma_f32 v[184:185], v[194:195], v[206:207], v[108:109]
	v_min_f32_e32 v180, 0x40e00000, v180
	v_min_f32_e32 v181, 0x40e00000, v181
	v_min_f32_e32 v184, 0x40e00000, v184
	v_min_f32_e32 v185, 0x40e00000, v185
	v_pk_fma_f32 v[194:195], v[196:197], v[208:209], v[96:97]
	v_pk_fma_f32 v[196:197], v[198:199], v[210:211], v[82:83]
	v_pk_fma_f32 v[198:199], v[200:201], v[212:213], v[78:79]
	v_pk_mul_f32 v[200:201], v[180:181], s[30:31] op_sel_hi:[1,0]
	v_pk_mul_f32 v[204:205], v[184:185], s[30:31] op_sel_hi:[1,0]
	v_exp_f32_e32 v200, v200
	v_exp_f32_e32 v201, v201
	v_exp_f32_e32 v204, v204
	v_exp_f32_e32 v205, v205
	v_min_f32_e32 v196, 0x40e00000, v196
	v_min_f32_e32 v197, 0x40e00000, v197
	v_pk_mul_f32 v[206:207], v[196:197], s[30:31] op_sel_hi:[1,0]
	v_pk_add_f32 v[200:201], v[200:201], 1.0 op_sel_hi:[1,0]
	v_exp_f32_e32 v206, v206
	v_exp_f32_e32 v207, v207
	v_pk_add_f32 v[204:205], v[204:205], 1.0 op_sel_hi:[1,0]
	v_rcp_f32_e32 v200, v200
	v_rcp_f32_e32 v201, v201
	v_rcp_f32_e32 v204, v204
	v_rcp_f32_e32 v205, v205
	v_pk_add_f32 v[206:207], v[206:207], 1.0 op_sel_hi:[1,0]
	v_med3_f32 v182, v182, s69, v193
	v_med3_f32 v183, v183, s69, v193
	v_med3_f32 v194, v194, s69, v193
	v_med3_f32 v195, v195, s69, v193
	v_rcp_f32_e32 v206, v206
	v_rcp_f32_e32 v207, v207
	v_pk_add_f32 v[182:183], v[182:183], 1.0 op_sel_hi:[1,0]
	v_pk_add_f32 v[194:195], v[194:195], 1.0 op_sel_hi:[1,0]
	v_pk_mul_f32 v[180:181], v[180:181], v[200:201]
	v_pk_mul_f32 v[184:185], v[184:185], v[204:205]
	v_pk_mul_f32 v[180:181], v[182:183], v[180:181]
	v_pk_mul_f32 v[182:183], v[194:195], v[184:185]
	v_pk_mul_f32 v[194:195], v[72:73], v[0:1] op_sel_hi:[1,0]
	v_med3_f32 v198, v198, s69, v193
	v_med3_f32 v199, v199, s69, v193
	v_pk_fma_f32 v[194:195], v[202:203], v[194:195], v[84:85]
	v_pk_add_f32 v[198:199], v[198:199], 1.0 op_sel_hi:[1,0]
	v_pk_mul_f32 v[196:197], v[196:197], v[206:207]
	v_min_f32_e32 v194, 0x40e00000, v194
	v_min_f32_e32 v195, 0x40e00000, v195
	v_pk_mul_f32 v[184:185], v[198:199], v[196:197]
	v_pk_mul_f32 v[196:197], v[194:195], s[30:31] op_sel_hi:[1,0]
	v_pk_mul_f32 v[198:199], v[76:77], v[0:1] op_sel_hi:[1,0]
	v_exp_f32_e32 v196, v196
	v_exp_f32_e32 v197, v197
	v_pk_fma_f32 v[148:149], v[148:149], v[198:199], v[80:81]
	v_max_f32_e64 v147, |v180|, |v181|
	v_med3_f32 v148, v148, s69, v193
	v_pk_add_f32 v[196:197], v[196:197], 1.0 op_sel_hi:[1,0]
	v_med3_f32 v149, v149, s69, v193
	v_rcp_f32_e32 v196, v196
	v_rcp_f32_e32 v197, v197
	v_pk_add_f32 v[148:149], v[148:149], 1.0 op_sel_hi:[1,0]
	v_max_f32_e64 v151, |v182|, |v183|
	v_max3_f32 v147, v147, 0, v151
	v_pk_mul_f32 v[194:195], v[194:195], v[196:197]
	v_max_f32_e64 v151, |v184|, |v185|
	v_pk_mul_f32 v[148:149], v[148:149], v[194:195]
	s_nop 0
	v_max_f32_e64 v0, |v148|, |v149|
	v_max3_f32 v0, v147, v151, v0
	v_mov_b32_e32 v147, v0
	s_nop 1
	v_permlane16_swap_b32_e32 v0, v147
	v_max_f32_e32 v0, v0, v147
	v_mov_b32_e32 v147, v0
	s_nop 1
	v_permlane32_swap_b32_e32 v0, v147
	v_max_f32_e32 v147, v0, v147
	s_and_saveexec_b64 s[40:41], s[4:5]
	s_cbranch_execz .LBB0_1221
	v_lshlrev_b64 v[194:195], 8, v[178:179]
	s_lshl_b32 s42, s10, 2
	v_lshl_add_u64 v[194:195], s[12:13], 0, v[194:195]
	s_ashr_i32 s43, s42, 31
	v_lshl_add_u64 v[194:195], s[42:43], 2, v[194:195]
	s_lshl_b32 s16, s62, 2
	v_lshl_add_u64 v[194:195], v[194:195], 0, s[16:17]
	global_store_dword v[194:195], v147, off

.Lkexit_1367:
.LBB0_1370:
	v_readlane_b32 s64, v252, 13
	s_ashr_i32 s39, s38, 31
	v_readlane_b32 s74, v252, 23
	v_readlane_b32 s75, v252, 24
	v_lshl_or_b32 v176, s14, 8, v228
	s_lshl_b64 s[0:1], s[38:39], 13
	s_mov_b64 s[62:63], s[74:75]
	s_add_u32 s38, s62, s0
	v_ashrrev_i32_e32 v177, 31, v176
	v_lshl_add_u32 v200, s16, 8, v1
	s_addc_u32 s39, s63, s1
	v_lshlrev_b64 v[66:67], 2, v[176:177]
	v_or_b32_e32 v212, 32, v200
	v_lshl_add_u64 v[70:71], s[38:39], 0, v[66:67]
	v_readlane_b32 s38, v252, 50
	v_ashrrev_i32_e32 v201, 31, v200
	v_or_b32_e32 v218, 16, v200
	v_ashrrev_i32_e32 v213, 31, v212
	v_readlane_b32 s39, v252, 51
	s_add_u32 s0, s38, s0
	v_lshlrev_b64 v[82:83], 2, v[200:201]
	v_ashrrev_i32_e32 v219, 31, v218
	v_lshlrev_b64 v[180:181], 2, v[212:213]
	s_addc_u32 s1, s39, s1
	v_lshl_add_u64 v[84:85], s[20:21], 0, v[82:83]
	v_lshlrev_b64 v[96:97], 2, v[218:219]
	v_lshl_add_u64 v[182:183], s[20:21], 0, v[180:181]
	v_lshl_add_u64 v[94:95], s[0:1], 0, v[66:67]
	global_load_dwordx4 v[86:89], v[70:71], off offset:16
	global_load_dwordx4 v[98:101], v[70:71], off
	global_load_dwordx4 v[90:93], v[94:95], off offset:16
	global_load_dwordx4 v[102:105], v[94:95], off
	global_load_dwordx4 v[66:69], v[70:71], off offset:528
	s_nop 0
	global_load_dwordx4 v[70:73], v[70:71], off offset:512
	v_lshl_add_u64 v[82:83], s[10:11], 0, v[82:83]
	v_lshl_add_u64 v[178:179], s[20:21], 0, v[96:97]
	v_lshl_add_u64 v[96:97], s[10:11], 0, v[96:97]
	v_lshl_add_u64 v[180:181], s[10:11], 0, v[180:181]
	v_or_b32_e32 v206, 48, v200
	global_load_dword v220, v[84:85], off
	global_load_dword v222, v[82:83], off
	global_load_dword v214, v[178:179], off
	global_load_dword v216, v[96:97], off
	global_load_dword v208, v[182:183], off
	global_load_dword v210, v[180:181], off
	global_load_dword v198, v[82:83], off offset:512
	global_load_dword v196, v[84:85], off offset:512
	v_add_u32_e32 v194, 0x90, v200
	v_add_u32_e32 v188, 0xa0, v200
	v_add_u32_e32 v182, 0xb0, v200
	v_ashrrev_i32_e32 v207, 31, v206
	v_ashrrev_i32_e32 v195, 31, v194
	v_ashrrev_i32_e32 v189, 31, v188
	v_ashrrev_i32_e32 v183, 31, v182
	v_lshlrev_b64 v[184:185], 2, v[206:207]
	v_lshlrev_b64 v[82:83], 2, v[194:195]
	v_lshlrev_b64 v[96:97], 2, v[188:189]
	v_lshlrev_b64 v[180:181], 2, v[182:183]
	v_lshl_add_u64 v[186:187], s[20:21], 0, v[184:185]
	v_lshl_add_u64 v[184:185], s[10:11], 0, v[184:185]
	v_lshl_add_u64 v[84:85], s[20:21], 0, v[82:83]
	v_lshl_add_u64 v[82:83], s[10:11], 0, v[82:83]
	v_lshl_add_u64 v[178:179], s[20:21], 0, v[96:97]
	v_lshl_add_u64 v[96:97], s[10:11], 0, v[96:97]
	v_lshl_add_u64 v[224:225], s[20:21], 0, v[180:181]
	v_lshl_add_u64 v[180:181], s[10:11], 0, v[180:181]
	global_load_dword v202, v[186:187], off
	global_load_dword v204, v[184:185], off
	global_load_dword v190, v[84:85], off
	global_load_dword v192, v[82:83], off
	s_nop 0
	global_load_dword v184, v[178:179], off
	global_load_dword v186, v[96:97], off
	s_nop 0
	global_load_dword v178, v[224:225], off
	s_nop 0
	global_load_dword v180, v[180:181], off
	s_nop 0
	global_load_dwordx4 v[82:85], v[94:95], off offset:528
	s_nop 0
	global_load_dwordx4 v[94:97], v[94:95], off offset:512
	v_cvt_f32_i32_e32 v159, v159
	v_cvt_f32_i32_e32 v158, v158
	v_cvt_f32_i32_e32 v157, v157
	v_cvt_f32_i32_e32 v156, v156
	v_cvt_f32_i32_e32 v161, v161
	v_cvt_f32_i32_e32 v160, v160
	v_cvt_f32_i32_e32 v155, v155
	v_cvt_f32_i32_e32 v154, v154
	v_lshlrev_b64 v[232:233], 8, v[200:201]
	v_readlane_b32 s65, v252, 14
	v_readlane_b32 s66, v252, 15
	v_readlane_b32 s67, v252, 16
	v_readlane_b32 s68, v252, 17
	v_readlane_b32 s69, v252, 18
	v_readlane_b32 s70, v252, 19
	v_readlane_b32 s71, v252, 20
	v_readlane_b32 s72, v252, 21
	v_readlane_b32 s73, v252, 22
	v_readlane_b32 s76, v252, 25
	v_readlane_b32 s77, v252, 26
	v_readlane_b32 s78, v252, 27
	v_readlane_b32 s79, v252, 28
	s_and_b64 vcc, exec, s[24:25]
	s_cbranch_vccz .Lepi_nb_1367
	s_barrier
.Lepi_nb_1367:
	s_waitcnt vmcnt(0)
	v_pk_mul_f32 v[238:239], v[92:93], v[222:223] op_sel_hi:[1,0]
	v_pk_mul_f32 v[224:225], v[102:103], v[222:223] op_sel_hi:[1,0]
	v_pk_mul_f32 v[234:235], v[104:105], v[222:223] op_sel_hi:[1,0]
	v_pk_mul_f32 v[236:237], v[90:91], v[222:223] op_sel_hi:[1,0]
	v_pk_fma_f32 v[158:159], v[158:159], v[224:225], v[98:99]
	v_pk_fma_f32 v[224:225], v[156:157], v[238:239], v[88:89]
	v_pk_fma_f32 v[160:161], v[160:161], v[234:235], v[100:101]
	v_pk_fma_f32 v[154:155], v[154:155], v[236:237], v[86:87]
	v_pk_mul_f32 v[224:225], v[220:221], v[224:225] op_sel_hi:[0,1]
	v_pk_mul_f32 v[156:157], v[220:221], v[158:159] op_sel_hi:[0,1]
	v_pk_mul_f32 v[158:159], v[220:221], v[160:161] op_sel_hi:[0,1]
	v_pk_mul_f32 v[160:161], v[220:221], v[154:155] op_sel_hi:[0,1]
	v_max_f32_e64 v155, |v224|, |v225|
	v_max_f32_e64 v0, |v156|, |v157|
	v_max_f32_e64 v154, |v158|, |v159|
	v_max3_f32 v155, |v160|, |v161|, v155
	v_max3_f32 v0, v0, v154, v155
	v_mov_b32_e32 v154, v0
	s_nop 1
	v_permlane16_swap_b32_e32 v0, v154
	v_max_f32_e32 v0, v0, v154
	v_mov_b32_e32 v154, v0
	s_nop 1
	v_permlane32_swap_b32_e32 v0, v154
	v_max_f32_e32 v179, v0, v154
	v_lshl_add_u64 v[154:155], s[12:13], 0, v[232:233]
	s_and_saveexec_b64 s[0:1], s[4:5]
	s_cbranch_execz .LBB0_1372
	s_lshl_b32 s38, s14, 3
	s_ashr_i32 s39, s38, 31
	v_lshl_add_u64 v[232:233], s[38:39], 2, v[154:155]
	s_lshl_b32 s16, s52, 2
	v_lshl_add_u64 v[232:233], v[232:233], 0, s[16:17]
	v_mul_f32_e32 v0, 0x3c010204, v179
	global_store_dword v[232:233], v0, off
